# speedup vs baseline: 1.0376x; 1.0208x over previous
.Lg_s3skip0:
	s_cmp_eq_u32 s10, 10
	s_cselect_b32 s32, s46, s32
	s_sub_u32 s18, s10, 4
	s_cmp_lt_u32 s18, s9
	s_cselect_b32 s19, s32, 0x80000000
	ds_read_b128 v[226:229], v245 offset:0
	s_add_u32 s32, s32, 0x40000
	v_readlane_b32 s13, v247, s18
	v_lshrrev_b32_e32 v249, 4, v1
	v_lshlrev_b32_e32 v249, 3, v249
	v_lshrrev_b32_e64 v249, v249, s13
	v_and_b32_e32 v249, 0xff, v249
	v_cmp_eq_u32_e32 vcc, 1, v249
	s_nop 1
	v_cndmask_b32_e32 v249, v255, v246, vcc
	s_waitcnt lgkmcnt(0)
	buffer_store_dwordx4 v[226:229], v249, s[28:31], s19 offen sc0 sc1
	s_add_u32 s10, s10, 1
	s_cmp_ge_u32 s10, s11
	s_cbranch_scc1 .Lg_end
	s_barrier
	s_cmp_ge_u32 s10, s11
	s_cbranch_scc1 .Lg_end

.Lg_s3skip1:
	s_cmp_eq_u32 s10, 10
	s_cselect_b32 s32, s46, s32
	s_sub_u32 s18, s10, 4
	s_cmp_lt_u32 s18, s9
	s_cselect_b32 s19, s32, 0x80000000
	ds_read_b128 v[226:229], v245 offset:4352
	s_add_u32 s32, s32, 0x40000
	v_readlane_b32 s13, v247, s18
	v_lshrrev_b32_e32 v249, 4, v1
	v_lshlrev_b32_e32 v249, 3, v249
	v_lshrrev_b32_e64 v249, v249, s13
	v_and_b32_e32 v249, 0xff, v249
	v_cmp_eq_u32_e32 vcc, 1, v249
	s_nop 1
	v_cndmask_b32_e32 v249, v255, v246, vcc
	s_waitcnt lgkmcnt(0)
	buffer_store_dwordx4 v[226:229], v249, s[28:31], s19 offen sc0 sc1
	s_add_u32 s10, s10, 1
	s_cmp_ge_u32 s10, s11
	s_cbranch_scc1 .Lg_end
	s_barrier
	s_cmp_lt_u32 s10, s11
	s_cbranch_scc1 .Lg_top
